# o8stage_na: neighbourhood-attention unit epilogue output bytes through a per-wave 2 KB LDS image, 2 dwordx4 stores per lane instead of 32 one-byte stores (loop-continuation wait vmcnt(32) -> vmcnt(2))
# baseline (speedup 1.0000x reference)
.LBB0_256:
	s_waitcnt vmcnt(2)
	v_mov_b64_e32 v[126:127], v[154:155]
	v_mov_b64_e32 v[122:123], v[158:159]
	v_mov_b64_e32 v[118:119], v[146:147]
	v_mov_b64_e32 v[114:115], v[150:151]
	v_mov_b64_e32 v[110:111], v[138:139]
	v_mov_b64_e32 v[106:107], v[142:143]
	v_mov_b64_e32 v[102:103], v[130:131]
	v_mov_b64_e32 v[98:99], v[134:135]
	s_mov_b32 s63, s65
	s_mov_b64 s[18:19], s[28:29]
	v_mov_b64_e32 v[128:129], v[156:157]
	v_mov_b64_e32 v[124:125], v[160:161]
	v_mov_b64_e32 v[120:121], v[148:149]
	v_mov_b64_e32 v[116:117], v[152:153]
	v_mov_b64_e32 v[112:113], v[140:141]
	v_mov_b64_e32 v[108:109], v[144:145]
	v_mov_b64_e32 v[104:105], v[132:133]
	v_mov_b64_e32 v[100:101], v[136:137]
	s_mov_b64 s[20:21], s[6:7]
	s_mov_b32 s62, s64
	s_cmpk_gt_i32 s61, 0x7ff
	s_mov_b64 s[4:5], -1
	s_cbranch_scc0 .LBB0_290

.LBB0_351:
	v_mul_f32_e32 v2, 0x41000000, v4
	v_mov_b32_e32 v4, v3
	v_add_u32_e32 v36, s16, v222
	v_cvt_pk_fp8_f32 v4, v2, 0
	v_mul_f32_e32 v2, 0x41000000, v20
	v_mov_b32_e32 v20, v3
	v_ashrrev_i32_e32 v37, 31, v36
	v_cvt_pk_fp8_f32 v20, v2, 0
	v_lshl_add_u64 v[18:19], v[196:197], 0, s[38:39]
	v_lshlrev_b64 v[38:39], 10, v[36:37]
	v_lshl_add_u64 v[38:39], v[18:19], 0, v[38:39]
	v_lshrrev_b32_e32 v249, 6, v0
	v_lshlrev_b32_e32 v249, 11, v249
	v_add_u32_e32 v249, 0x1a000, v249
	v_readfirstlane_b32 s100, v38
	v_readfirstlane_b32 s101, v39
	v_and_b32_e32 v247, 63, v0
	v_and_b32_e32 v246, 31, v247
	v_lshrrev_b32_e32 v248, 5, v247
	v_lshl_add_u32 v246, v248, 8, v246
	v_add_u32_e32 v246, v249, v246
	v_lshrrev_b32_e32 v248, 2, v247
	v_lshlrev_b32_e32 v248, 10, v248
	v_and_b32_e32 v250, 3, v247
	v_lshl_add_u32 v248, v250, 4, v248
	v_lshl_add_u32 v247, v247, 4, v249
	v_mov_b32_e32 v249, 0
	v_lshl_add_u64 v[248:249], v[248:249], 0, s[100:101]
	ds_write_b8 v246, v4 offset:0
	ds_write_b8 v246, v20 offset:32
	v_mul_f32_e32 v2, 0x41000000, v5
	v_mov_b32_e32 v20, v3
	v_add_u32_e32 v38, 1, v36
	v_cvt_pk_fp8_f32 v20, v2, 0
	v_mul_f32_e32 v2, 0x41000000, v21
	v_mov_b32_e32 v21, v3
	v_ashrrev_i32_e32 v39, 31, v38
	v_cvt_pk_fp8_f32 v21, v2, 0
	v_lshlrev_b64 v[4:5], 10, v[38:39]
	v_lshl_add_u64 v[4:5], v[18:19], 0, v[4:5]
	v_mul_f32_e32 v2, 0x41000000, v6
	v_mov_b32_e32 v6, v3
	ds_write_b8 v246, v20 offset:64
	ds_write_b8 v246, v21 offset:96
	v_add_u32_e32 v4, 2, v36
	v_cvt_pk_fp8_f32 v6, v2, 0
	v_mul_f32_e32 v2, 0x41000000, v22
	v_mov_b32_e32 v20, v3
	v_ashrrev_i32_e32 v5, 31, v4
	v_cvt_pk_fp8_f32 v20, v2, 0
	v_lshlrev_b64 v[4:5], 10, v[4:5]
	v_lshl_add_u64 v[4:5], v[18:19], 0, v[4:5]
	ds_write_b8 v246, v6 offset:128
	ds_write_b8 v246, v20 offset:160
	v_mul_f32_e32 v2, 0x41000000, v7
	v_mov_b32_e32 v6, v3
	v_add_u32_e32 v4, 3, v36
	v_cvt_pk_fp8_f32 v6, v2, 0
	v_mul_f32_e32 v2, 0x41000000, v23
	v_mov_b32_e32 v7, v3
	v_ashrrev_i32_e32 v5, 31, v4
	v_cvt_pk_fp8_f32 v7, v2, 0
	v_lshlrev_b64 v[4:5], 10, v[4:5]
	v_lshl_add_u64 v[4:5], v[18:19], 0, v[4:5]
	ds_write_b8 v246, v6 offset:192
	ds_write_b8 v246, v7 offset:224
	v_mul_f32_e32 v2, 0x41000000, v8
	v_mov_b32_e32 v6, v3
	v_add_u32_e32 v4, 8, v36
	v_cvt_pk_fp8_f32 v6, v2, 0
	v_mul_f32_e32 v2, 0x41000000, v24
	v_mov_b32_e32 v7, v3
	v_ashrrev_i32_e32 v5, 31, v4
	v_cvt_pk_fp8_f32 v7, v2, 0
	v_lshlrev_b64 v[4:5], 10, v[4:5]
	v_lshl_add_u64 v[4:5], v[18:19], 0, v[4:5]
	ds_write_b8 v246, v6 offset:512
	ds_write_b8 v246, v7 offset:544
	v_mul_f32_e32 v2, 0x41000000, v9
	v_mov_b32_e32 v6, v3
	v_add_u32_e32 v4, 9, v36
	v_cvt_pk_fp8_f32 v6, v2, 0
	v_mul_f32_e32 v2, 0x41000000, v25
	v_mov_b32_e32 v7, v3
	v_ashrrev_i32_e32 v5, 31, v4
	v_cvt_pk_fp8_f32 v7, v2, 0
	v_lshlrev_b64 v[4:5], 10, v[4:5]
	v_lshl_add_u64 v[4:5], v[18:19], 0, v[4:5]
	ds_write_b8 v246, v6 offset:576
	ds_write_b8 v246, v7 offset:608
	v_mul_f32_e32 v2, 0x41000000, v10
	v_mov_b32_e32 v6, v3
	v_add_u32_e32 v4, 10, v36
	v_cvt_pk_fp8_f32 v6, v2, 0
	v_mul_f32_e32 v2, 0x41000000, v26
	v_mov_b32_e32 v7, v3
	v_ashrrev_i32_e32 v5, 31, v4
	v_cvt_pk_fp8_f32 v7, v2, 0
	v_lshlrev_b64 v[4:5], 10, v[4:5]
	v_lshl_add_u64 v[4:5], v[18:19], 0, v[4:5]
	ds_write_b8 v246, v6 offset:640
	ds_write_b8 v246, v7 offset:672
	v_mul_f32_e32 v2, 0x41000000, v11
	v_mov_b32_e32 v6, v3
	v_add_u32_e32 v4, 11, v36
	v_cvt_pk_fp8_f32 v6, v2, 0
	v_mul_f32_e32 v2, 0x41000000, v27
	v_mov_b32_e32 v7, v3
	v_ashrrev_i32_e32 v5, 31, v4
	v_cvt_pk_fp8_f32 v7, v2, 0
	v_lshlrev_b64 v[4:5], 10, v[4:5]
	v_lshl_add_u64 v[4:5], v[18:19], 0, v[4:5]
	ds_write_b8 v246, v6 offset:704
	ds_write_b8 v246, v7 offset:736
	v_mul_f32_e32 v2, 0x41000000, v12
	v_mov_b32_e32 v6, v3
	v_add_u32_e32 v4, 16, v36
	v_cvt_pk_fp8_f32 v6, v2, 0
	v_mul_f32_e32 v2, 0x41000000, v28
	v_mov_b32_e32 v7, v3
	v_ashrrev_i32_e32 v5, 31, v4
	v_cvt_pk_fp8_f32 v7, v2, 0
	v_lshlrev_b64 v[4:5], 10, v[4:5]
	v_lshl_add_u64 v[4:5], v[18:19], 0, v[4:5]
	ds_write_b8 v246, v6 offset:1024
	ds_write_b8 v246, v7 offset:1056
	v_mul_f32_e32 v2, 0x41000000, v13
	v_mov_b32_e32 v6, v3
	v_add_u32_e32 v4, 17, v36
	v_cvt_pk_fp8_f32 v6, v2, 0
	v_mul_f32_e32 v2, 0x41000000, v29
	v_mov_b32_e32 v7, v3
	v_ashrrev_i32_e32 v5, 31, v4
	v_cvt_pk_fp8_f32 v7, v2, 0
	v_lshlrev_b64 v[4:5], 10, v[4:5]
	v_lshl_add_u64 v[4:5], v[18:19], 0, v[4:5]
	ds_write_b8 v246, v6 offset:1088
	ds_write_b8 v246, v7 offset:1120
	v_mul_f32_e32 v2, 0x41000000, v14
	v_mov_b32_e32 v6, v3
	v_add_u32_e32 v4, 18, v36
	v_cvt_pk_fp8_f32 v6, v2, 0
	v_mul_f32_e32 v2, 0x41000000, v30
	v_mov_b32_e32 v7, v3
	v_ashrrev_i32_e32 v5, 31, v4
	v_cvt_pk_fp8_f32 v7, v2, 0
	v_lshlrev_b64 v[4:5], 10, v[4:5]
	v_lshl_add_u64 v[4:5], v[18:19], 0, v[4:5]
	ds_write_b8 v246, v6 offset:1152
	ds_write_b8 v246, v7 offset:1184
	v_mul_f32_e32 v2, 0x41000000, v15
	v_mov_b32_e32 v6, v3
	v_add_u32_e32 v4, 19, v36
	v_cvt_pk_fp8_f32 v6, v2, 0
	v_mul_f32_e32 v2, 0x41000000, v31
	v_mov_b32_e32 v7, v3
	v_ashrrev_i32_e32 v5, 31, v4
	v_cvt_pk_fp8_f32 v7, v2, 0
	v_lshlrev_b64 v[4:5], 10, v[4:5]
	v_lshl_add_u64 v[4:5], v[18:19], 0, v[4:5]
	ds_write_b8 v246, v6 offset:1216
	ds_write_b8 v246, v7 offset:1248
	v_mul_f32_e32 v2, 0x41000000, v16
	v_mov_b32_e32 v6, v3
	v_add_u32_e32 v4, 24, v36
	v_cvt_pk_fp8_f32 v6, v2, 0
	v_mul_f32_e32 v2, 0x41000000, v32
	v_mov_b32_e32 v7, v3
	v_ashrrev_i32_e32 v5, 31, v4
	v_cvt_pk_fp8_f32 v7, v2, 0
	v_lshlrev_b64 v[4:5], 10, v[4:5]
	v_lshl_add_u64 v[4:5], v[18:19], 0, v[4:5]
	ds_write_b8 v246, v6 offset:1536
	ds_write_b8 v246, v7 offset:1568
	v_mul_f32_e32 v2, 0x41000000, v17
	v_mov_b32_e32 v6, v3
	v_add_u32_e32 v4, 25, v36
	v_cvt_pk_fp8_f32 v6, v2, 0
	v_mul_f32_e32 v2, 0x41000000, v33
	v_mov_b32_e32 v7, v3
	v_ashrrev_i32_e32 v5, 31, v4
	v_cvt_pk_fp8_f32 v7, v2, 0
	v_lshlrev_b64 v[4:5], 10, v[4:5]
	v_lshl_add_u64 v[4:5], v[18:19], 0, v[4:5]
	ds_write_b8 v246, v6 offset:1600
	ds_write_b8 v246, v7 offset:1632
	v_mul_f32_e32 v2, 0x41000000, v48
	v_mov_b32_e32 v6, v3
	v_add_u32_e32 v4, 26, v36
	v_cvt_pk_fp8_f32 v6, v2, 0
	v_mul_f32_e32 v2, 0x41000000, v34
	v_mov_b32_e32 v7, v3
	v_ashrrev_i32_e32 v5, 31, v4
	v_cvt_pk_fp8_f32 v7, v2, 0
	v_lshlrev_b64 v[4:5], 10, v[4:5]
	v_lshl_add_u64 v[4:5], v[18:19], 0, v[4:5]
	ds_write_b8 v246, v6 offset:1664
	ds_write_b8 v246, v7 offset:1696
	v_mul_f32_e32 v2, 0x41000000, v49
	v_mov_b32_e32 v6, v3
	v_add_u32_e32 v4, 27, v36
	v_cvt_pk_fp8_f32 v6, v2, 0
	v_ashrrev_i32_e32 v5, 31, v4
	v_lshlrev_b64 v[4:5], 10, v[4:5]
	v_lshl_add_u64 v[4:5], v[18:19], 0, v[4:5]
	ds_write_b8 v246, v6 offset:1728
	v_mul_f32_e32 v2, 0x41000000, v35
	v_mov_b32_e32 v6, v3
	v_cvt_pk_fp8_f32 v6, v2, 0
	s_add_i32 s61, s61, s22
	s_add_i32 s60, s60, s22
	s_cmpk_gt_i32 s61, 0x81f
	ds_write_b8 v246, v6 offset:1760
	s_waitcnt lgkmcnt(0)
	s_mov_b32 s100, 0x4000
	s_mov_b32 s101, 0
	ds_read_b128 v[250:253], v247
	s_waitcnt lgkmcnt(0)
	global_store_dwordx4 v[248:249], v[250:253], off
	v_lshl_add_u64 v[248:249], v[248:249], 0, s[100:101]
	s_nop 1
	ds_read_b128 v[250:253], v247 offset:1024
	s_waitcnt lgkmcnt(0)
	global_store_dwordx4 v[248:249], v[250:253], off
	s_nop 1
	s_cbranch_scc0 .LBB0_256
	s_branch .LBB0_353
